# baseline (speedup 1.0000x reference)
.LBB1_90:
	s_and_b64 vcc, exec, s[4:5]
	s_cbranch_vccz .LBB1_94
	s_cmpk_ge_u32 s2, 0x300
	s_cbranch_scc1 .LBB1_94
	s_load_dwordx4 s[4:7], s[0:1], 0x38
	v_lshrrev_b32_e32 v1, 6, v0
	v_and_b32_e32 v2, 63, v0
	v_readfirstlane_b32 s10, v1
	v_lshlrev_b32_e32 v3, 5, v2
	v_lshlrev_b32_e32 v4, 4, v2
	s_sub_u32 s11, s2, 0x100
	s_lshl_b32 s11, s11, 3
	s_add_u32 s11, s11, s10
	s_lshl_b32 s12, s11, 14
	s_mul_i32 s13, s11, 0x2100
	s_waitcnt lgkmcnt(0)
	s_add_u32 s16, s4, s12
	s_addc_u32 s17, s5, 0
	s_add_u32 s14, s6, s13
	s_addc_u32 s15, s7, 0
	s_sub_u32 s14, s14, 0x100000
	s_subb_u32 s15, s15, 0
	s_add_u32 s18, s16, 0x1000
	s_addc_u32 s19, s17, 0
	s_add_u32 s20, s18, 0x2000
	s_addc_u32 s21, s19, 0
	s_add_u32 s22, s14, 0x1000
	s_addc_u32 s23, s15, 0
	global_load_dwordx4 v[8:11], v3, s[18:19] offset:-4096 nt
	global_load_dwordx4 v[12:15], v3, s[18:19] offset:-4080 nt
	global_load_dwordx4 v[16:19], v3, s[18:19] offset:-2048 nt
	global_load_dwordx4 v[20:23], v3, s[18:19] offset:-2032 nt
	global_load_dwordx4 v[24:27], v3, s[18:19] offset:0 nt
	global_load_dwordx4 v[28:31], v3, s[18:19] offset:16 nt
	global_load_dwordx4 v[32:35], v3, s[18:19] offset:2048 nt
	global_load_dwordx4 v[36:39], v3, s[18:19] offset:2064 nt
	global_load_dwordx4 v[40:43], v3, s[20:21] offset:-4096 nt
	global_load_dwordx4 v[44:47], v3, s[20:21] offset:-4080 nt
	global_load_dwordx4 v[48:51], v3, s[20:21] offset:-2048 nt
	global_load_dwordx4 v[52:55], v3, s[20:21] offset:-2032 nt
	global_load_dwordx4 v[56:59], v3, s[20:21] offset:0 nt
	global_load_dwordx4 v[60:63], v3, s[20:21] offset:16 nt
	global_load_dwordx4 v[64:67], v3, s[20:21] offset:2048 nt
	global_load_dwordx4 v[68:71], v3, s[20:21] offset:2064 nt
	s_waitcnt vmcnt(14)
	v_cvt_pk_f16_f32 v8, v8, v9
	v_cvt_pk_f16_f32 v9, v10, v11
	v_cvt_pk_f16_f32 v10, v12, v13
	v_cvt_pk_f16_f32 v11, v14, v15
	global_store_dwordx4 v4, v[8:11], s[22:23] offset:-4096 sc1
	s_waitcnt vmcnt(13)
	v_cvt_pk_f16_f32 v16, v16, v17
	v_cvt_pk_f16_f32 v17, v18, v19
	v_cvt_pk_f16_f32 v18, v20, v21
	v_cvt_pk_f16_f32 v19, v22, v23
	global_store_dwordx4 v4, v[16:19], s[22:23] offset:-3072 sc1
	s_waitcnt vmcnt(12)
	v_cvt_pk_f16_f32 v24, v24, v25
	v_cvt_pk_f16_f32 v25, v26, v27
	v_cvt_pk_f16_f32 v26, v28, v29
	v_cvt_pk_f16_f32 v27, v30, v31
	global_store_dwordx4 v4, v[24:27], s[22:23] offset:-2048 sc1
	s_waitcnt vmcnt(11)
	v_cvt_pk_f16_f32 v32, v32, v33
	v_cvt_pk_f16_f32 v33, v34, v35
	v_cvt_pk_f16_f32 v34, v36, v37
	v_cvt_pk_f16_f32 v35, v38, v39
	global_store_dwordx4 v4, v[32:35], s[22:23] offset:-1024 sc1
	s_waitcnt vmcnt(10)
	v_cvt_pk_f16_f32 v40, v40, v41
	v_cvt_pk_f16_f32 v41, v42, v43
	v_cvt_pk_f16_f32 v42, v44, v45
	v_cvt_pk_f16_f32 v43, v46, v47
	global_store_dwordx4 v4, v[40:43], s[22:23] offset:128 sc1
	s_waitcnt vmcnt(9)
	v_cvt_pk_f16_f32 v48, v48, v49
	v_cvt_pk_f16_f32 v49, v50, v51
	v_cvt_pk_f16_f32 v50, v52, v53
	v_cvt_pk_f16_f32 v51, v54, v55
	global_store_dwordx4 v4, v[48:51], s[22:23] offset:1152 sc1
	s_waitcnt vmcnt(8)
	v_cvt_pk_f16_f32 v56, v56, v57
	v_cvt_pk_f16_f32 v57, v58, v59
	v_cvt_pk_f16_f32 v58, v60, v61
	v_cvt_pk_f16_f32 v59, v62, v63
	global_store_dwordx4 v4, v[56:59], s[22:23] offset:2176 sc1
	s_waitcnt vmcnt(7)
	v_cvt_pk_f16_f32 v64, v64, v65
	v_cvt_pk_f16_f32 v65, v66, v67
	v_cvt_pk_f16_f32 v66, v68, v69
	v_cvt_pk_f16_f32 v67, v70, v71
	global_store_dwordx4 v4, v[64:67], s[22:23] offset:3200 sc1

.Las_set:
	s_cmp_ge_i32 s48, s47
	s_cbranch_scc1 .LBB2_78
	s_load_dword s13, s[0:1], 0x38
	s_load_dwordx2 s[2:3], s[0:1], 0x30
	s_load_dwordx8 s[4:11], s[0:1], 0x0
	v_bfe_u32 v1, v0, 4, 2
	v_lshrrev_b32_e32 v2, 5, v0
	s_waitcnt lgkmcnt(0)
	s_sub_u32 s6, s6, 0x100000
	s_subb_u32 s7, s7, 0
	s_lshr_b32 s49, s13, 3
	s_bfe_u32 s1, s12, 0x10006
	v_and_or_b32 v2, v2, 4, v1
	v_lshrrev_b32_e32 v5, 7, v0
	s_cmpk_lt_u32 s12, 0x80
	v_lshlrev_b32_e32 v2, 4, v2
	v_lshlrev_b32_e32 v3, 3, v0
	s_movk_i32 s0, 0x78
	v_bfe_u32 v4, v0, 4, 3
	v_bitop3_b32 v5, v5, v0, 7 bitop3:0x78
	v_lshlrev_b32_e32 v6, 6, v0
	s_cselect_b64 s[12:13], -1, 0
	v_bitop3_b32 v2, v2, v3, s0 bitop3:0x78
	v_xor_b32_e32 v5, v5, v4
	s_lshl_b32 s0, s1, 6
	v_lshlrev_b32_e32 v4, 2, v1
	v_lshlrev_b32_e32 v1, 11, v1
	v_and_b32_e32 v6, 0x300, v6
	v_and_b32_e32 v8, 8, v3
	v_lshrrev_b32_e32 v101, 4, v0
	v_and_b32_e32 v103, 15, v0
	v_lshrrev_b32_e32 v124, 3, v0
	v_lshl_add_u32 v125, v0, 4, 0
	v_or3_b32 v1, v1, v6, v8
	v_bfe_u32 v6, v0, 1, 3
	v_or_b32_e32 v0, s0, v4
	v_and_b32_e32 v7, 0xe0, v3
	v_lshl_add_u32 v100, v0, 1, 0
	s_lshl_b32 s1, s1, 7
	v_and_b32_e32 v0, 16, v3
	v_or_b32_e32 v3, s1, v0
	v_bitop3_b32 v0, s1, v7, v0 bitop3:0x36
	v_or_b32_e32 v127, v0, v1
	v_bitop3_b32 v0, v3, v7, 32 bitop3:0x36
	v_or_b32_e32 v128, v0, v1
	v_bitop3_b32 v0, v3, v7, 64 bitop3:0x36
	s_movk_i32 s1, 0x60
	v_or_b32_e32 v129, v0, v1
	v_bitop3_b32 v0, v3, v7, s1 bitop3:0x36
	s_add_i32 s1, s23, 15
	s_lshr_b32 s1, s1, 4
	v_or_b32_e32 v130, v0, v1
	s_add_i32 s1, s39, s1
	v_cvt_f32_i32_e32 v0, s39
	s_add_i32 s1, s1, -1
	v_cvt_f32_i32_e32 v1, s1
	s_add_i32 s14, s25, 15
	v_rcp_iflag_f32_e32 v144, v0
	s_lshr_b32 s14, s14, 4
	v_add_f32_e32 v0, 0.5, v1
	v_cvt_f32_i32_e32 v1, s40
	s_add_i32 s14, s40, s14
	s_add_i32 s14, s14, -1
	v_mul_f32_e32 v0, v144, v0
	v_cvt_i32_f32_e32 v0, v0
	v_cvt_f32_i32_e32 v7, s14
	v_rcp_iflag_f32_e32 v145, v1
	s_add_i32 s16, s27, 15
	s_lshr_b32 s16, s16, 4
	v_cvt_f32_i32_e32 v1, s41
	s_add_i32 s16, s41, s16
	v_readfirstlane_b32 s1, v0
	v_add_f32_e32 v0, 0.5, v7
	s_add_i32 s16, s16, -1
	s_add_i32 s17, s29, 15
	s_add_i32 s18, s31, 15
	s_add_i32 s19, s33, 15
	s_add_i32 s20, s35, 15
	s_add_i32 s21, s38, 15
	v_mul_f32_e32 v0, v145, v0
	s_lshr_b32 s17, s17, 4
	s_lshr_b32 s18, s18, 4
	s_lshr_b32 s19, s19, 4
	s_lshr_b32 s20, s20, 4
	s_lshr_b32 s21, s21, 4
	v_cvt_i32_f32_e32 v0, v0
	v_cvt_f32_i32_e32 v7, s16
	s_add_i32 s17, s42, s17
	s_add_i32 s18, s43, s18
	s_add_i32 s19, s44, s19
	s_add_i32 s20, s45, s20
	s_add_i32 s21, s46, s21
	v_rcp_iflag_f32_e32 v146, v1
	s_add_i32 s50, 0, 0xe000
	s_lshl_b32 s52, s39, 4
	s_lshl_b32 s53, s40, 4
	s_lshl_b32 s54, s41, 4
	s_add_i32 s17, s17, -1
	s_lshl_b32 s55, s42, 4
	s_add_i32 s18, s18, -1
	s_lshl_b32 s56, s43, 4
	s_add_i32 s19, s19, -1
	s_lshl_b32 s57, s44, 4
	s_add_i32 s20, s20, -1
	s_lshl_b32 s58, s45, 4
	s_add_i32 s21, s21, -1
	s_lshl_b32 s59, s46, 4
	s_cmp_gt_i32 s23, 0
	v_cvt_f32_i32_e32 v1, s42
	s_cselect_b32 s60, s1, 0
	v_readfirstlane_b32 s1, v0
	v_add_f32_e32 v0, 0.5, v7
	v_mul_f32_e32 v0, v146, v0
	v_cvt_i32_f32_e32 v0, v0
	v_cvt_f32_i32_e32 v7, s17
	v_rcp_iflag_f32_e32 v147, v1
	s_cmp_gt_i32 s25, 0
	v_cvt_f32_i32_e32 v1, s43
	s_cselect_b32 s61, s1, 0
	v_readfirstlane_b32 s1, v0
	v_add_f32_e32 v0, 0.5, v7
	v_mul_f32_e32 v0, v147, v0
	v_cvt_i32_f32_e32 v0, v0
	v_cvt_f32_i32_e32 v7, s18
	v_rcp_iflag_f32_e32 v148, v1
	s_cmp_gt_i32 s27, 0
	v_cvt_f32_i32_e32 v1, s44
	s_cselect_b32 s62, s1, 0
	v_readfirstlane_b32 s1, v0
	v_add_f32_e32 v0, 0.5, v7
	v_mul_f32_e32 v0, v148, v0
	v_cvt_i32_f32_e32 v0, v0
	v_cvt_f32_i32_e32 v7, s19
	v_rcp_iflag_f32_e32 v149, v1
	s_cmp_gt_i32 s29, 0
	v_cvt_f32_i32_e32 v1, s45
	s_cselect_b32 s63, s1, 0
	v_readfirstlane_b32 s1, v0
	v_add_f32_e32 v0, 0.5, v7
	v_mul_f32_e32 v0, v149, v0
	v_cvt_i32_f32_e32 v0, v0
	v_cvt_f32_i32_e32 v7, s20
	v_rcp_iflag_f32_e32 v150, v1
	s_cmp_gt_i32 s31, 0
	s_cselect_b32 s64, s1, 0
	v_readfirstlane_b32 s1, v0
	v_add_f32_e32 v0, 0.5, v7
	v_mul_f32_e32 v0, v150, v0
	v_cvt_i32_f32_e32 v0, v0
	v_cvt_f32_i32_e32 v1, s46
	s_cmp_gt_i32 s33, 0
	s_cselect_b32 s65, s1, 0
	v_readfirstlane_b32 s1, v0
	v_cvt_f32_i32_e32 v0, s21
	v_rcp_iflag_f32_e32 v151, v1
	v_mov_b32_e32 v97, 0
	v_mul_u32_u24_e32 v96, 0x1080, v101
	v_add_f32_e32 v0, 0.5, v0
	v_mul_f32_e32 v0, v151, v0
	v_cvt_i32_f32_e32 v7, v0
	v_lshlrev_b32_e32 v0, 4, v5
	v_mov_b32_e32 v1, v97
	v_lshl_add_u64 v[98:99], s[6:7], 0, v[96:97]
	s_cmp_gt_i32 s35, 0
	v_lshl_add_u64 v[104:105], s[4:5], 0, v[0:1]
	s_mov_b64 s[4:5], 0x80
	v_lshl_add_u32 v96, v2, 1, v96
	v_lshl_add_u32 v8, v103, 4, 0
	v_mul_u32_u24_e32 v3, 0x110, v101
	s_cselect_b32 s66, s1, 0
	s_cmp_gt_i32 s38, 0
	v_readfirstlane_b32 s1, v7
	v_lshl_add_u64 v[106:107], v[104:105], 0, s[4:5]
	v_lshl_add_u64 v[0:1], s[6:7], 0, v[96:97]
	s_mov_b64 s[4:5], 0x42000
	s_mov_b32 s15, 0
	v_lshlrev_b32_e32 v126, 7, v103
	v_lshlrev_b32_e32 v102, 3, v103
	v_add_u32_e32 v131, s50, v127
	v_add_u32_e32 v132, s50, v128
	v_add_u32_e32 v133, s50, v129
	v_add_u32_e32 v134, s50, v130
	s_movk_i32 s51, 0x110
	v_or_b32_e32 v135, 16, v101
	v_or_b32_e32 v136, 32, v101
	v_or_b32_e32 v137, 48, v101
	v_or_b32_e32 v138, 64, v101
	v_or_b32_e32 v139, 0x50, v101
	v_or_b32_e32 v140, 0x60, v101
	v_or_b32_e32 v141, 0x70, v101
	v_or_b32_e32 v142, 0x80, v101
	v_or_b32_e32 v143, 0x90, v101
	v_bitop3_b32 v152, v6, v101, 3 bitop3:0x78
	s_mul_i32 s67, s52, s60
	s_mul_i32 s68, s53, s61
	s_mul_i32 s69, s54, s62
	s_mul_i32 s70, s55, s63
	s_mul_i32 s71, s56, s64
	s_mul_i32 s72, s57, s65
	s_mul_i32 s73, s58, s66
	s_cselect_b32 s74, s1, 0
	v_lshl_add_u64 v[108:109], v[0:1], 0, s[4:5]
	s_lshl_b32 s6, s0, 2
	v_lshlrev_b32_e32 v153, 2, v4
	v_lshlrev_b32_e32 v96, 1, v2
	s_mov_b64 s[16:17], 0x10800
	s_mov_b64 s[18:19], 0x21000
	s_mov_b64 s[20:21], 0x31800
	s_mov_b32 s22, 0x3f3504f3
	s_mov_b32 s75, 0x3ea7ba05
	s_mov_b32 s24, 0xbfba00e3
	s_mov_b32 s26, 0x3f87dc22
	s_mov_b32 s28, 0x3fb5f0e3
	s_brev_b32 s76, -2
	v_add_u32_e32 v154, v8, v3
	s_movk_i32 s77, 0x1080
	s_mov_b32 s30, 0xbe91a98e
	s_mov_b32 s34, 0x3e827906
	s_branch .LBB2_3

.LBB2_39:
	s_lshl_b32 s36, s79, 4
	v_mul_lo_u32 v155, s36, v1
	v_add_u32_e32 v120, v155, v124
	v_cmp_gt_i32_e32 vcc, s80, v120
	s_lshl_b32 s81, s37, 13
	s_nop 0
	v_cndmask_b32_e32 v1, 0, v120, vcc
	v_add_u32_e32 v2, s81, v1
	v_add_u32_e32 v1, 32, v120
	v_cmp_gt_i32_e32 vcc, s80, v1
	v_ashrrev_i32_e32 v3, 31, v2
	v_lshl_add_u64 v[2:3], v[2:3], 2, s[2:3]
	v_cndmask_b32_e32 v1, 0, v1, vcc
	v_add_u32_e32 v4, s81, v1
	v_add_u32_e32 v1, 64, v120
	v_cmp_gt_i32_e32 vcc, s80, v1
	v_ashrrev_i32_e32 v5, 31, v4
	s_barrier
	v_cndmask_b32_e32 v1, 0, v1, vcc
	v_add_u32_e32 v6, s81, v1
	v_add_u32_e32 v1, 0x60, v120
	v_cmp_gt_i32_e32 vcc, s80, v1
	v_ashrrev_i32_e32 v7, 31, v6
	s_nop 0
	v_cndmask_b32_e32 v1, 0, v1, vcc
	v_add_u32_e32 v8, s81, v1
	v_ashrrev_i32_e32 v9, 31, v8
	v_lshl_add_u64 v[4:5], v[4:5], 2, s[2:3]
	v_lshl_add_u64 v[6:7], v[6:7], 2, s[2:3]
	v_lshl_add_u64 v[8:9], v[8:9], 2, s[2:3]
	global_load_dword v16, v[2:3], off
	global_load_dword v18, v[4:5], off
	global_load_dword v20, v[6:7], off
	global_load_dword v22, v[8:9], off
	v_lshlrev_b32_e32 v24, 7, v0
	s_add_i32 s0, s79, 1
	s_mul_i32 s14, s37, 0x420000
	v_add_u32_e32 v2, 0x5000, v125
	s_ashr_i32 s37, s0, 1
	v_lshl_add_u64 v[0:1], v[98:99], 0, s[14:15]
	v_ashrrev_i32_e32 v25, 31, v24
	v_add_u32_e32 v3, 0x6000, v125
	v_readfirstlane_b32 s83, v2
	v_lshl_add_u64 v[0:1], v[24:25], 1, v[0:1]
	s_add_u32 s0, s8, s81
	v_add_u32_e32 v4, 0x7000, v125
	v_add_u32_e32 v5, 0x8000, v125
	v_readfirstlane_b32 s84, v3
	v_lshlrev_b64 v[2:3], 2, v[24:25]
	s_addc_u32 s1, s9, 0
	v_lshl_add_u64 v[0:1], v[0:1], 0, v[96:97]
	s_mov_b32 m0, s83
	s_mov_b32 s7, s15
	v_readfirstlane_b32 s85, v4
	v_readfirstlane_b32 s86, v5
	v_lshl_add_u64 v[2:3], s[0:1], 0, v[2:3]
	global_load_lds_dwordx4 v[0:1], off sc1
	v_lshl_add_u64 v[4:5], v[0:1], 0, s[16:17]
	s_mov_b32 m0, s84
	v_lshl_add_u64 v[6:7], v[0:1], 0, s[18:19]
	v_lshl_add_u64 v[26:27], v[0:1], 0, s[20:21]
	v_lshl_add_u64 v[0:1], v[2:3], 0, s[6:7]
	global_load_lds_dwordx4 v[4:5], off sc1
	s_mov_b32 m0, s85
	v_readfirstlane_b32 s82, v125
	v_readfirstlane_b32 s0, v0
	v_readfirstlane_b32 s1, v1
	global_load_lds_dwordx4 v[6:7], off sc1
	s_mov_b32 m0, s86
	s_nop 2
	global_load_dwordx4 v[12:15], v153, s[0:1]
	global_load_dwordx4 v[8:11], v153, s[0:1] offset:64
	global_load_dwordx4 v[4:7], v153, s[0:1] offset:128
	global_load_dwordx4 v[0:3], v153, s[0:1] offset:192
	v_lshlrev_b64 v[110:111], 1, v[24:25]
	global_load_lds_dwordx4 v[26:27], off sc1
	s_mov_b32 m0, s82
	s_waitcnt vmcnt(0)
	v_ashrrev_i32_e32 v17, 31, v16
	v_lshlrev_b64 v[16:17], 11, v[16:17]
	v_lshl_add_u64 v[26:27], v[104:105], 0, v[16:17]
	v_ashrrev_i32_e32 v19, 31, v18
	global_load_lds_dwordx4 v[26:27], off sc1
	v_add_u32_e32 v26, 0x1000, v125
	v_ashrrev_i32_e32 v21, 31, v20
	v_lshlrev_b64 v[18:19], 11, v[18:19]
	v_readfirstlane_b32 s0, v26
	v_add_u32_e32 v26, 0x2000, v125
	v_ashrrev_i32_e32 v23, 31, v22
	v_lshlrev_b64 v[20:21], 11, v[20:21]
	v_lshl_add_u64 v[28:29], v[104:105], 0, v[18:19]
	s_mov_b32 m0, s0
	v_readfirstlane_b32 s0, v26
	v_add_u32_e32 v26, 0x3000, v125
	v_lshlrev_b64 v[22:23], 11, v[22:23]
	v_lshl_add_u64 v[30:31], v[104:105], 0, v[20:21]
	global_load_lds_dwordx4 v[28:29], off sc1
	s_mov_b32 m0, s0
	v_readfirstlane_b32 s0, v26
	v_lshl_add_u64 v[32:33], v[104:105], 0, v[22:23]
	global_load_lds_dwordx4 v[30:31], off sc1
	s_mov_b32 m0, s0
	s_and_b64 s[0:1], s[12:13], exec
	global_load_lds_dwordx4 v[32:33], off sc1
	s_cselect_b32 s7, 0, s37
	v_bitop3_b32 v27, s7, v152, 1 bitop3:0x6c
	v_lshl_or_b32 v26, s7, 11, v126
	v_lshlrev_b32_e32 v159, 4, v27
	s_cmp_lt_i32 s79, 9
	s_mov_b64 s[0:1], -1
	v_add_u32_e32 v156, 0, v26
	v_lshl_add_u64 v[112:113], v[106:107], 0, v[16:17]
	v_lshl_add_u64 v[114:115], v[106:107], 0, v[18:19]
	v_lshl_add_u64 v[116:117], v[106:107], 0, v[20:21]
	v_lshl_add_u64 v[118:119], v[106:107], 0, v[22:23]
	v_xor_b32_e32 v160, 16, v159
	v_xor_b32_e32 v158, 64, v159
	v_xor_b32_e32 v157, 0x50, v159
	s_cbranch_scc0 .LBB2_43
	v_lshl_add_u64 v[16:17], s[14:15], 0, v[110:111]
	v_lshl_add_u64 v[80:81], v[108:109], 0, v[16:17]
	v_mov_b32_e32 v16, 0
	s_mov_b32 s82, 1
	s_mov_b64 s[0:1], 0
	v_mov_b32_e32 v17, v16
	v_mov_b32_e32 v18, v16
	v_mov_b32_e32 v19, v16
	v_mov_b32_e32 v20, v16
	v_mov_b32_e32 v21, v16
	v_mov_b32_e32 v22, v16
	v_mov_b32_e32 v23, v16
	v_mov_b32_e32 v24, v16
	v_mov_b32_e32 v25, v16
	v_mov_b32_e32 v26, v16
	v_mov_b32_e32 v27, v16
	v_mov_b32_e32 v28, v16
	v_mov_b32_e32 v29, v16
	v_mov_b32_e32 v30, v16
	v_mov_b32_e32 v31, v16
	v_mov_b32_e32 v32, v16
	v_mov_b32_e32 v33, v16
	v_mov_b32_e32 v34, v16
	v_mov_b32_e32 v35, v16
	v_mov_b32_e32 v36, v16
	v_mov_b32_e32 v37, v16
	v_mov_b32_e32 v38, v16
	v_mov_b32_e32 v39, v16
	v_mov_b32_e32 v40, v16
	v_mov_b32_e32 v41, v16
	v_mov_b32_e32 v42, v16
	v_mov_b32_e32 v43, v16
	v_mov_b32_e32 v44, v16
	v_mov_b32_e32 v45, v16
	v_mov_b32_e32 v46, v16
	v_mov_b32_e32 v47, v16
	v_mov_b32_e32 v48, v16
	v_mov_b32_e32 v49, v16
	v_mov_b32_e32 v50, v16
	v_mov_b32_e32 v51, v16
	v_mov_b32_e32 v52, v16
	v_mov_b32_e32 v53, v16
	v_mov_b32_e32 v54, v16
	v_mov_b32_e32 v55, v16
	v_mov_b32_e32 v56, v16
	v_mov_b32_e32 v57, v16
	v_mov_b32_e32 v58, v16
	v_mov_b32_e32 v59, v16
	v_mov_b32_e32 v60, v16
	v_mov_b32_e32 v61, v16
	v_mov_b32_e32 v62, v16
	v_mov_b32_e32 v63, v16
	v_mov_b32_e32 v64, v16
	v_mov_b32_e32 v65, v16
	v_mov_b32_e32 v66, v16
	v_mov_b32_e32 v67, v16
	v_mov_b32_e32 v68, v16
	v_mov_b32_e32 v69, v16
	v_mov_b32_e32 v70, v16
	v_mov_b32_e32 v71, v16
	v_mov_b32_e32 v72, v16
	v_mov_b32_e32 v73, v16
	v_mov_b32_e32 v74, v16
	v_mov_b32_e32 v75, v16
	v_mov_b32_e32 v76, v16
	v_mov_b32_e32 v77, v16
	v_mov_b32_e32 v78, v16
	v_mov_b32_e32 v79, v16
